# v79 + selected-branch tile loop: the first staging block of each iteration issued behind tile 0's K fragment reads instead of at the loop head
# baseline (speedup 1.0000x reference)
; #define LAS __attribute__((address_space(3)))
; __device__ __forceinline__ void attn_qk2m(LAS unsigned char* Kb, const bf16x8 (&q)[2][2], int fr, int g4, const float (&cinit)[2], f32x4 (&s)[2][4]) {
;     bf16x8 kf[4][2];
; #pragma unroll
;     for (int c = 0; c < 4; ++c)
; #pragma unroll
;         for (int ks = 0; ks < 2; ++ks) kf[c][ks] = *(const LAS bf16x8*)(Kb + pg8::lds_byte(16 * c + fr, 32 * ks + 8 * g4));
;     __builtin_amdgcn_sched_barrier(0);
;     f32x4 ci[2];
; #pragma unroll
;     for (int rb = 0; rb < 2; ++rb) ci[rb] = (f32x4){cinit[rb], cinit[rb], cinit[rb], cinit[rb]};
; #pragma unroll
;     for (int c = 0; c < 4; ++c) {
; #pragma unroll
;         for (int ks = 0; ks < 2; ++ks) {
; #pragma unroll
;             for (int rb = 0; rb < 2; ++rb) s[rb][c] = __builtin_amdgcn_mfma_f32_16x16x32_bf16(kf[c][ks], q[rb][ks], ks == 0 ? ci[rb] : s[rb][c], 0, 0, 0);
;         }
;     }
; }
; __device__ __forceinline__ void attn_step2x_nomax(LAS unsigned char* Vb, f32x4 (&s)[2][4], AttnRow (&st)[2], int kbase, int g4, const int (&lo)[2], const int (&hi)[2], const unsigned (&enm)[2], bool emask,
;                                                   int vlane, int swz, const bf16x8 onesf) {
;     if (emask) {
; #pragma unroll
;         for (int rb = 0; rb < 2; ++rb)
; #pragma unroll
;             for (int c = 0; c < 4; ++c)
; #pragma unroll
;                 for (int i = 0; i < 4; ++i) { const int key = kbase + 16 * c + 4 * g4 + i; if (key < lo[rb] || key > hi[rb]) s[rb][c][i] = -INFINITY; }
;     }
.LBB0_2087:
	s_and_b32 s0, s33, 28
	s_lshl_b32 s0, 1, s0
	s_waitcnt lgkmcnt(0)
	v_and_b32_e32 v1, s0, v4
	v_cmp_ne_u32_e32 vcc, 0, v1
	v_and_b32_e32 v1, s0, v5
	v_cmp_ne_u32_e64 s[0:1], 0, v1
	s_add_i32 s78, s2, s77
	s_or_b64 s[80:81], vcc, s[0:1]
	s_cmp_eq_u64 s[80:81], 0
	s_cbranch_scc1 .Lslc_nm_t0_none
	s_cmp_eq_u64 vcc, 0
	s_cbranch_scc1 .Lslc_nm_rb1_t0
	s_cmp_eq_u64 s[0:1], 0
	s_cbranch_scc1 .Lslc_nm_rb0_t0
	v_lshl_add_u32 v1, s76, 14, v220
	ds_read_b128 v[66:69], v1
	ds_read_b128 v[70:73], v1 offset:1024
	ds_read_b128 v[78:81], v1 offset:2048
	ds_read_b128 v[82:85], v1 offset:3072
	ds_read_b128 v[86:89], v1 offset:4096
	ds_read_b128 v[98:101], v1 offset:5120
	ds_read_b128 v[102:105], v1 offset:6144
	ds_read_b128 v[110:113], v1 offset:7168
	s_add_i32 s80, s77, 1
	s_cmp_gt_u32 s80, s83
	s_cbranch_scc1 .Lslc_nm_dma0_skip_d
	s_add_u32 s80, s74, 0x1fb08000
	s_addc_u32 s81, s75, 0
	s_add_i32 m0, s32, 0x0
	s_nop 0
	global_load_lds_dwordx4 v150, s[80:81]
	s_add_u32 s80, s74, 0x20b08000
	s_addc_u32 s81, s75, 0
	s_add_i32 m0, s32, 0x8000
	s_nop 0
	global_load_lds_dwordx4 v152, s[80:81]
.Lslc_nm_dma0_skip_d:
	v_cndmask_b32_e64 v114, v248, 0, vcc
	v_cndmask_b32_e64 v118, v248, 0, s[0:1]
	v_mov_b32_e32 v115, v114
	v_mov_b32_e32 v116, v114
	v_mov_b32_e32 v117, v114
	v_mov_b32_e32 v119, v118
	v_mov_b32_e32 v120, v118
	v_mov_b32_e32 v121, v118
	s_waitcnt lgkmcnt(0)
	v_mfma_f32_16x16x32_bf16 v[74:77], v[66:69], v[10:13], v[114:117]
	s_cmp_lg_u32 s78, 3
	v_mfma_f32_16x16x32_bf16 v[66:69], v[66:69], v[18:21], v[118:121]
	v_mfma_f32_16x16x32_bf16 v[94:97], v[70:73], v[14:17], v[74:77]
	v_mfma_f32_16x16x32_bf16 v[74:77], v[70:73], v[22:25], v[66:69]
	v_mfma_f32_16x16x32_bf16 v[66:69], v[78:81], v[10:13], v[114:117]
	v_mfma_f32_16x16x32_bf16 v[70:73], v[78:81], v[18:21], v[118:121]
	v_mfma_f32_16x16x32_bf16 v[90:93], v[82:85], v[14:17], v[66:69]
	v_mfma_f32_16x16x32_bf16 v[66:69], v[86:89], v[10:13], v[114:117]
	v_mfma_f32_16x16x32_bf16 v[78:81], v[86:89], v[18:21], v[118:121]
	v_mfma_f32_16x16x32_bf16 v[86:89], v[98:101], v[14:17], v[66:69]
	v_mfma_f32_16x16x32_bf16 v[66:69], v[98:101], v[22:25], v[78:81]
	v_mfma_f32_16x16x32_bf16 v[78:81], v[102:105], v[10:13], v[114:117]
	v_mfma_f32_16x16x32_bf16 v[98:101], v[102:105], v[18:21], v[118:121]
	v_mfma_f32_16x16x32_bf16 v[70:73], v[82:85], v[22:25], v[70:73]
	v_mfma_f32_16x16x32_bf16 v[82:85], v[110:113], v[14:17], v[78:81]
	v_mfma_f32_16x16x32_bf16 v[78:81], v[110:113], v[22:25], v[98:101]
	s_cbranch_scc1 .LBB0_2092
	v_mov_b32_e32 v2, s96
	s_nop 5
	v_cndmask_b32_e64 v78, v78, v2, s[66:67]
	v_cndmask_b32_e64 v79, v79, v246, s[68:69]
	v_cndmask_b32_e64 v80, v80, v246, s[70:71]
	s_and_saveexec_b64 s[0:1], s[72:73]
	v_mov_b32_e32 v81, s96
	s_or_b64 exec, exec, s[0:1]
	v_mov_b32_e32 v2, s96
	v_cndmask_b32_e64 v1, v94, v2, s[8:9]
	v_cndmask_b32_e64 v94, v1, v94, s[10:11]
	v_cndmask_b32_e64 v1, v74, v2, s[42:43]
	v_cndmask_b32_e64 v95, v246, v95, s[10:11]
	v_cndmask_b32_e64 v96, v96, v246, s[12:13]
	v_cndmask_b32_e64 v97, v97, v246, s[14:15]
	v_cndmask_b32_e64 v90, v90, v2, s[16:17]
	v_cndmask_b32_e64 v91, v91, v246, s[18:19]
	v_cndmask_b32_e64 v92, v92, v246, s[20:21]
	v_cndmask_b32_e64 v93, v93, v246, s[22:23]
	v_cndmask_b32_e64 v86, v86, v2, s[24:25]
	v_cndmask_b32_e64 v87, v87, v246, s[26:27]
	v_cndmask_b32_e64 v88, v88, v246, s[28:29]
	v_cndmask_b32_e64 v89, v89, v246, s[30:31]
	v_cndmask_b32_e64 v82, v82, v2, s[34:35]
	v_cndmask_b32_e64 v83, v83, v246, s[36:37]
	v_cndmask_b32_e64 v84, v84, v246, s[38:39]
	v_cndmask_b32_e64 v85, v85, v246, s[40:41]
	v_cndmask_b32_e64 v75, v246, v75, s[44:45]
	v_cndmask_b32_e64 v74, v1, v74, s[44:45]
	v_cndmask_b32_e64 v76, v76, v246, s[46:47]
	v_cndmask_b32_e64 v77, v77, v246, s[48:49]
	v_cndmask_b32_e64 v70, v70, v2, s[50:51]
	v_cndmask_b32_e64 v71, v71, v246, s[52:53]
	v_cndmask_b32_e64 v72, v72, v246, s[54:55]
	v_cndmask_b32_e64 v73, v73, v246, s[56:57]
	v_cndmask_b32_e64 v66, v66, v2, s[58:59]
	v_cndmask_b32_e64 v67, v67, v246, s[60:61]
	v_cndmask_b32_e64 v68, v68, v246, s[62:63]
	v_cndmask_b32_e64 v69, v69, v246, s[64:65]

.Lslc_nm_t0_none:
	s_add_i32 s80, s77, 1
	s_cmp_gt_u32 s80, s83
	s_cbranch_scc1 .Lslc_nm_dma0_skip_n
	s_add_u32 s80, s74, 0x1fb08000
	s_addc_u32 s81, s75, 0
	s_add_i32 m0, s32, 0x0
	s_nop 0
	global_load_lds_dwordx4 v150, s[80:81]
	s_add_u32 s80, s74, 0x20b08000
	s_addc_u32 s81, s75, 0
	s_add_i32 m0, s32, 0x8000
	s_nop 0
	global_load_lds_dwordx4 v152, s[80:81]

; #define LAS __attribute__((address_space(3)))
; __device__ __forceinline__ u32x4 pack8m(const f32x4 v0, const f32x4 v1) { u32x4 w; w.x = cvtpk_m(v0[0], v0[1]); w.y = cvtpk_m(v0[2], v0[3]); w.z = cvtpk_m(v1[0], v1[1]); w.w = cvtpk_m(v1[2], v1[3]); return w; }
; __device__ __forceinline__ void attn_exp1(f32x4 (&s)[4], unsigned enm, bf16x8 (&pb)[2]) {
; #pragma unroll
;     for (int c = 0; c < 4; ++c)
; #pragma unroll
;         for (int i = 0; i < 4; ++i) s[c][i] = __builtin_amdgcn_exp2f(s[c][i]);
; #pragma unroll
;     for (int ks = 0; ks < 2; ++ks) { u32x4 pw = pack8m(s[2 * ks], s[2 * ks + 1]); pw.x &= enm; pw.y &= enm; pw.z &= enm; pw.w &= enm; pb[ks] = __builtin_bit_cast(bf16x8, pw); }
; }
; __device__ __forceinline__ void attn_pv1(LAS unsigned char* Vb, const bf16x8 (&pb)[2], int vlane, int swz, const bf16x8 onesf, AttnRow& st) {
; #pragma unroll
;     for (int ks = 0; ks < 2; ++ks) {
; #pragma unroll
;         for (int dt = 0; dt < 4; ++dt) {
;             LAS unsigned char* a0 = Vb + vlane + (2 * ks) * 2048 + ((dt ^ swz) * 32);
;             const bf16x8 vf = tr_frag(a0, a0 + 2048);
;             st.o[dt] = __builtin_amdgcn_mfma_f32_16x16x32_bf16(vf, pb[ks], st.o[dt], 0, 0, 0);
;         }
;         st.ol = __builtin_amdgcn_mfma_f32_16x16x32_bf16(onesf, pb[ks], st.ol, 0, 0, 0);
;     }
; }
.Lslc_nm_rb0_t0:
	v_lshl_add_u32 v1, s76, 14, v220
	ds_read_b128 v[66:69], v1
	ds_read_b128 v[70:73], v1 offset:1024
	ds_read_b128 v[74:77], v1 offset:2048
	ds_read_b128 v[78:81], v1 offset:3072
	ds_read_b128 v[82:85], v1 offset:4096
	ds_read_b128 v[86:89], v1 offset:5120
	ds_read_b128 v[90:93], v1 offset:6144
	ds_read_b128 v[94:97], v1 offset:7168
	s_add_i32 s80, s77, 1
	s_cmp_gt_u32 s80, s83
	s_cbranch_scc1 .Lslc_nm_dma0_skip_a
	s_add_u32 s80, s74, 0x1fb08000
	s_addc_u32 s81, s75, 0
	s_add_i32 m0, s32, 0x0
	s_nop 0
	global_load_lds_dwordx4 v150, s[80:81]
	s_add_u32 s80, s74, 0x20b08000
	s_addc_u32 s81, s75, 0
	s_add_i32 m0, s32, 0x8000
	s_nop 0
	global_load_lds_dwordx4 v152, s[80:81]
.Lslc_nm_dma0_skip_a:
	v_cndmask_b32_e64 v98, v248, 0, vcc
	v_mov_b32_e32 v99, v98
	v_mov_b32_e32 v100, v98
	v_mov_b32_e32 v101, v98
	s_lshl_b32 s0, s76, 13
	s_cmp_eq_u32 s76, 0
	s_mov_b32 s1, 0x8000
	s_cselect_b32 s1, s1, 0x10000
	s_add_i32 s1, s1, s0
	v_add_u32_e32 v1, s1, v214
	v_add_u32_e32 v2, v1, v221
	v_add_u32_e32 v107, v1, v222
	v_add_u32_e32 v109, v1, v223
	v_add_u32_e32 v1, v1, v224
	s_waitcnt lgkmcnt(6)
	v_mfma_f32_16x16x32_bf16 v[102:105], v[66:69], v[10:13], v[98:101]
	s_waitcnt lgkmcnt(4)
	v_mfma_f32_16x16x32_bf16 v[110:113], v[74:77], v[10:13], v[98:101]
	v_mfma_f32_16x16x32_bf16 v[102:105], v[70:73], v[14:17], v[102:105]
	v_mfma_f32_16x16x32_bf16 v[110:113], v[78:81], v[14:17], v[110:113]
	s_waitcnt lgkmcnt(2)
	v_mfma_f32_16x16x32_bf16 v[114:117], v[82:85], v[10:13], v[98:101]
	s_waitcnt lgkmcnt(0)
	v_mfma_f32_16x16x32_bf16 v[118:121], v[90:93], v[10:13], v[98:101]
	v_mfma_f32_16x16x32_bf16 v[114:117], v[86:89], v[14:17], v[114:117]
	v_mfma_f32_16x16x32_bf16 v[118:121], v[94:97], v[14:17], v[118:121]
	ds_read_b64_tr_b16 v[66:67], v2
	ds_read_b64_tr_b16 v[68:69], v2 offset:2048
	ds_read_b64_tr_b16 v[70:71], v107
	ds_read_b64_tr_b16 v[72:73], v107 offset:2048
	ds_read_b64_tr_b16 v[74:75], v109
	ds_read_b64_tr_b16 v[76:77], v109 offset:2048
	ds_read_b64_tr_b16 v[78:79], v1
	ds_read_b64_tr_b16 v[80:81], v1 offset:2048
	v_exp_f32_e32 v102, v102
	v_exp_f32_e32 v103, v103
	v_exp_f32_e32 v104, v104
	v_exp_f32_e32 v105, v105
	v_exp_f32_e32 v110, v110
	v_exp_f32_e32 v111, v111
	v_exp_f32_e32 v112, v112
	v_exp_f32_e32 v113, v113
	v_cvt_pk_bf16_f32 v98, v102, v103
	v_cvt_pk_bf16_f32 v99, v104, v105
	v_cvt_pk_bf16_f32 v100, v110, v111
	v_cvt_pk_bf16_f32 v101, v112, v113
	s_waitcnt lgkmcnt(7)
	ds_read_b64_tr_b16 v[82:83], v2 offset:4096
	ds_read_b64_tr_b16 v[84:85], v2 offset:6144
	ds_read_b64_tr_b16 v[86:87], v107 offset:4096
	ds_read_b64_tr_b16 v[88:89], v107 offset:6144
	ds_read_b64_tr_b16 v[90:91], v109 offset:4096
	ds_read_b64_tr_b16 v[92:93], v109 offset:6144
	ds_read_b64_tr_b16 v[94:95], v1 offset:4096
	ds_read_b64_tr_b16 v[96:97], v1 offset:6144
	s_waitcnt lgkmcnt(14)
	v_mfma_f32_16x16x32_bf16 v[46:49], v[66:69], v[98:101], v[46:49]
	v_exp_f32_e32 v114, v114
	v_exp_f32_e32 v115, v115
	s_waitcnt lgkmcnt(12)
	v_mfma_f32_16x16x32_bf16 v[50:53], v[70:73], v[98:101], v[50:53]
	v_exp_f32_e32 v116, v116
	v_exp_f32_e32 v117, v117
	s_waitcnt lgkmcnt(10)
	v_mfma_f32_16x16x32_bf16 v[54:57], v[74:77], v[98:101], v[54:57]
	v_exp_f32_e32 v118, v118
	v_exp_f32_e32 v119, v119
	s_waitcnt lgkmcnt(8)
	v_mfma_f32_16x16x32_bf16 v[58:61], v[78:81], v[98:101], v[58:61]
	v_exp_f32_e32 v120, v120
	v_exp_f32_e32 v121, v121
	v_cvt_pk_bf16_f32 v102, v114, v115
	v_cvt_pk_bf16_f32 v103, v116, v117
	v_cvt_pk_bf16_f32 v104, v118, v119
	v_mfma_f32_16x16x32_bf16 v[62:65], v[6:9], v[98:101], v[62:65]
	v_cvt_pk_bf16_f32 v105, v120, v121
	s_waitcnt lgkmcnt(6)
	s_nop 0
	v_mfma_f32_16x16x32_bf16 v[46:49], v[82:85], v[102:105], v[46:49]
	s_waitcnt lgkmcnt(4)
	v_mfma_f32_16x16x32_bf16 v[50:53], v[86:89], v[102:105], v[50:53]
	s_waitcnt lgkmcnt(2)
	v_mfma_f32_16x16x32_bf16 v[54:57], v[90:93], v[102:105], v[54:57]
	s_waitcnt lgkmcnt(0)
	v_mfma_f32_16x16x32_bf16 v[58:61], v[94:97], v[102:105], v[58:61]
	v_mfma_f32_16x16x32_bf16 v[62:65], v[6:9], v[102:105], v[62:65]
	s_branch .LBB0_2093

; #define LAS __attribute__((address_space(3)))
; __device__ __forceinline__ u32x4 pack8m(const f32x4 v0, const f32x4 v1) { u32x4 w; w.x = cvtpk_m(v0[0], v0[1]); w.y = cvtpk_m(v0[2], v0[3]); w.z = cvtpk_m(v1[0], v1[1]); w.w = cvtpk_m(v1[2], v1[3]); return w; }
; __device__ __forceinline__ void attn_exp1(f32x4 (&s)[4], unsigned enm, bf16x8 (&pb)[2]) {
; #pragma unroll
;     for (int c = 0; c < 4; ++c)
; #pragma unroll
;         for (int i = 0; i < 4; ++i) s[c][i] = __builtin_amdgcn_exp2f(s[c][i]);
; #pragma unroll
;     for (int ks = 0; ks < 2; ++ks) { u32x4 pw = pack8m(s[2 * ks], s[2 * ks + 1]); pw.x &= enm; pw.y &= enm; pw.z &= enm; pw.w &= enm; pb[ks] = __builtin_bit_cast(bf16x8, pw); }
; }
; __device__ __forceinline__ void attn_pv1(LAS unsigned char* Vb, const bf16x8 (&pb)[2], int vlane, int swz, const bf16x8 onesf, AttnRow& st) {
; #pragma unroll
;     for (int ks = 0; ks < 2; ++ks) {
; #pragma unroll
;         for (int dt = 0; dt < 4; ++dt) {
;             LAS unsigned char* a0 = Vb + vlane + (2 * ks) * 2048 + ((dt ^ swz) * 32);
;             const bf16x8 vf = tr_frag(a0, a0 + 2048);
;             st.o[dt] = __builtin_amdgcn_mfma_f32_16x16x32_bf16(vf, pb[ks], st.o[dt], 0, 0, 0);
;         }
;         st.ol = __builtin_amdgcn_mfma_f32_16x16x32_bf16(onesf, pb[ks], st.ol, 0, 0, 0);
;     }
; }
.Lslc_nm_dma0_skip_b:
	v_cndmask_b32_e64 v98, v248, 0, s[0:1]
	v_mov_b32_e32 v99, v98
	v_mov_b32_e32 v100, v98
	v_mov_b32_e32 v101, v98
	s_lshl_b32 s0, s76, 13
	s_cmp_eq_u32 s76, 0
	s_mov_b32 s1, 0x8000
	s_cselect_b32 s1, s1, 0x10000
	s_add_i32 s1, s1, s0
	v_add_u32_e32 v1, s1, v214
	v_add_u32_e32 v2, v1, v221
	v_add_u32_e32 v107, v1, v222
	v_add_u32_e32 v109, v1, v223
	v_add_u32_e32 v1, v1, v224
	s_waitcnt lgkmcnt(6)
	v_mfma_f32_16x16x32_bf16 v[102:105], v[66:69], v[18:21], v[98:101]
	s_waitcnt lgkmcnt(4)
	v_mfma_f32_16x16x32_bf16 v[110:113], v[74:77], v[18:21], v[98:101]
	v_mfma_f32_16x16x32_bf16 v[102:105], v[70:73], v[22:25], v[102:105]
	v_mfma_f32_16x16x32_bf16 v[110:113], v[78:81], v[22:25], v[110:113]
	s_waitcnt lgkmcnt(2)
	v_mfma_f32_16x16x32_bf16 v[114:117], v[82:85], v[18:21], v[98:101]
	s_waitcnt lgkmcnt(0)
	v_mfma_f32_16x16x32_bf16 v[118:121], v[90:93], v[18:21], v[98:101]
	v_mfma_f32_16x16x32_bf16 v[114:117], v[86:89], v[22:25], v[114:117]
	v_mfma_f32_16x16x32_bf16 v[118:121], v[94:97], v[22:25], v[118:121]
	ds_read_b64_tr_b16 v[66:67], v2
	ds_read_b64_tr_b16 v[68:69], v2 offset:2048
	ds_read_b64_tr_b16 v[70:71], v107
	ds_read_b64_tr_b16 v[72:73], v107 offset:2048
	ds_read_b64_tr_b16 v[74:75], v109
	ds_read_b64_tr_b16 v[76:77], v109 offset:2048
	ds_read_b64_tr_b16 v[78:79], v1
	ds_read_b64_tr_b16 v[80:81], v1 offset:2048
	v_exp_f32_e32 v102, v102
	v_exp_f32_e32 v103, v103
	v_exp_f32_e32 v104, v104
	v_exp_f32_e32 v105, v105
	v_exp_f32_e32 v110, v110
	v_exp_f32_e32 v111, v111
	v_exp_f32_e32 v112, v112
	v_exp_f32_e32 v113, v113
	v_cvt_pk_bf16_f32 v98, v102, v103
	v_cvt_pk_bf16_f32 v99, v104, v105
	v_cvt_pk_bf16_f32 v100, v110, v111
	v_cvt_pk_bf16_f32 v101, v112, v113
	s_waitcnt lgkmcnt(7)
	ds_read_b64_tr_b16 v[82:83], v2 offset:4096
	ds_read_b64_tr_b16 v[84:85], v2 offset:6144
	ds_read_b64_tr_b16 v[86:87], v107 offset:4096
	ds_read_b64_tr_b16 v[88:89], v107 offset:6144
	ds_read_b64_tr_b16 v[90:91], v109 offset:4096
	ds_read_b64_tr_b16 v[92:93], v109 offset:6144
	ds_read_b64_tr_b16 v[94:95], v1 offset:4096
	ds_read_b64_tr_b16 v[96:97], v1 offset:6144
	s_waitcnt lgkmcnt(14)
	v_mfma_f32_16x16x32_bf16 v[42:45], v[66:69], v[98:101], v[42:45]
	v_exp_f32_e32 v114, v114
	v_exp_f32_e32 v115, v115
	s_waitcnt lgkmcnt(12)
	v_mfma_f32_16x16x32_bf16 v[38:41], v[70:73], v[98:101], v[38:41]
	v_exp_f32_e32 v116, v116
	v_exp_f32_e32 v117, v117
	s_waitcnt lgkmcnt(10)
	v_mfma_f32_16x16x32_bf16 v[30:33], v[74:77], v[98:101], v[30:33]
	v_exp_f32_e32 v118, v118
	v_exp_f32_e32 v119, v119
	s_waitcnt lgkmcnt(8)
	v_mfma_f32_16x16x32_bf16 v[26:29], v[78:81], v[98:101], v[26:29]
	v_exp_f32_e32 v120, v120
	v_exp_f32_e32 v121, v121
	v_cvt_pk_bf16_f32 v102, v114, v115
	v_cvt_pk_bf16_f32 v103, v116, v117
	v_cvt_pk_bf16_f32 v104, v118, v119
	v_mfma_f32_16x16x32_bf16 v[34:37], v[6:9], v[98:101], v[34:37]
	v_cvt_pk_bf16_f32 v105, v120, v121
	s_waitcnt lgkmcnt(6)
	s_nop 0
	v_mfma_f32_16x16x32_bf16 v[42:45], v[82:85], v[102:105], v[42:45]
	s_waitcnt lgkmcnt(4)
	v_mfma_f32_16x16x32_bf16 v[38:41], v[86:89], v[102:105], v[38:41]
	s_waitcnt lgkmcnt(2)
	v_mfma_f32_16x16x32_bf16 v[30:33], v[90:93], v[102:105], v[30:33]
	s_waitcnt lgkmcnt(0)
	v_mfma_f32_16x16x32_bf16 v[26:29], v[94:97], v[102:105], v[26:29]
	v_mfma_f32_16x16x32_bf16 v[34:37], v[6:9], v[102:105], v[34:37]
	s_branch .LBB0_2093
